# final-norm output: gfinal gain loads hoisted ahead of the row stores (was load->vmcnt(0)->store x8); on top of B3 load batching, conversion cache policies, A1/retention epilogue hoists
# baseline (speedup 1.0000x reference)
.LBB0_1869:
	s_and_b64 vcc, exec, s[12:13]
	s_cbranch_vccz .LBB0_1871
	global_load_dwordx4 v[208:211], v[38:39], off
	global_load_dwordx4 v[212:215], v[38:39], off offset:1024
	global_load_dwordx4 v[216:219], v[38:39], off offset:2048
	global_load_dwordx4 v[224:227], v[38:39], off offset:3072
	global_load_dwordx4 v[228:231], v[42:43], off
	global_load_dwordx4 v[232:235], v[46:47], off
	global_load_dwordx4 v[236:239], v[50:51], off
	global_load_dwordx4 v[240:243], v[58:59], off
	s_nop 0
	s_ashr_i32 s9, s8, 31
	v_readlane_b32 s36, v252, 24
	s_lshl_b64 s[12:13], s[8:9], 13
	v_readlane_b32 s48, v252, 36
	v_readlane_b32 s49, v252, 37
	s_add_u32 s12, s48, s12
	v_pk_mul_f32 v[124:125], v[124:125], v[152:153] op_sel_hi:[1,0]
	v_pk_mul_f32 v[158:159], v[126:127], v[152:153] op_sel_hi:[1,0]
	s_addc_u32 s13, s49, s13
	v_pk_mul_f32 v[120:121], v[120:121], v[152:153] op_sel_hi:[1,0]
	v_readlane_b32 s37, v252, 25
	v_readlane_b32 s38, v252, 26
	v_readlane_b32 s39, v252, 27
	v_readlane_b32 s40, v252, 28
	v_readlane_b32 s41, v252, 29
	v_readlane_b32 s42, v252, 30
	v_readlane_b32 s43, v252, 31
	v_readlane_b32 s44, v252, 32
	v_readlane_b32 s45, v252, 33
	v_readlane_b32 s46, v252, 34
	v_readlane_b32 s47, v252, 35
	v_readlane_b32 s50, v252, 38
	v_readlane_b32 s51, v252, 39
	s_waitcnt vmcnt(7)
	v_pk_mul_f32 v[126:127], v[124:125], v[210:211]
	v_pk_mul_f32 v[124:125], v[158:159], v[208:209]
	v_lshlrev_b32_e32 v156, 4, v0
	global_store_dwordx4 v156, v[124:127], s[12:13]
	s_nop 0
	v_pk_mul_f32 v[154:155], v[122:123], v[152:153] op_sel_hi:[1,0]
	s_waitcnt vmcnt(7)
	v_pk_mul_f32 v[122:123], v[120:121], v[214:215]
	v_pk_mul_f32 v[120:121], v[154:155], v[212:213]
	global_store_dwordx4 v156, v[120:123], s[12:13] offset:1024
	s_nop 0
	v_pk_mul_f32 v[124:125], v[128:129], v[152:153] op_sel_hi:[1,0]
	v_pk_mul_f32 v[126:127], v[130:131], v[152:153] op_sel_hi:[1,0]
	s_waitcnt vmcnt(7)
	v_pk_mul_f32 v[122:123], v[124:125], v[218:219]
	v_pk_mul_f32 v[120:121], v[126:127], v[216:217]
	global_store_dwordx4 v156, v[120:123], s[12:13] offset:2048
	s_nop 0
	v_pk_mul_f32 v[124:125], v[132:133], v[152:153] op_sel_hi:[1,0]
	v_pk_mul_f32 v[126:127], v[134:135], v[152:153] op_sel_hi:[1,0]
	s_waitcnt vmcnt(7)
	v_pk_mul_f32 v[122:123], v[124:125], v[226:227]
	v_pk_mul_f32 v[120:121], v[126:127], v[224:225]
	global_store_dwordx4 v156, v[120:123], s[12:13] offset:3072
	s_nop 0
	v_pk_mul_f32 v[124:125], v[136:137], v[152:153] op_sel_hi:[1,0]
	v_pk_mul_f32 v[126:127], v[138:139], v[152:153] op_sel_hi:[1,0]
	s_waitcnt vmcnt(7)
	v_pk_mul_f32 v[122:123], v[124:125], v[230:231]
	v_pk_mul_f32 v[120:121], v[126:127], v[228:229]
	v_lshlrev_b32_e32 v124, 4, v40
	global_store_dwordx4 v124, v[120:123], s[12:13]
	s_nop 0
	v_pk_mul_f32 v[124:125], v[140:141], v[152:153] op_sel_hi:[1,0]
	v_pk_mul_f32 v[126:127], v[142:143], v[152:153] op_sel_hi:[1,0]
	s_waitcnt vmcnt(7)
	v_pk_mul_f32 v[122:123], v[124:125], v[234:235]
	v_pk_mul_f32 v[120:121], v[126:127], v[232:233]
	v_lshlrev_b32_e32 v124, 4, v44
	global_store_dwordx4 v124, v[120:123], s[12:13]
	s_nop 0
	v_pk_mul_f32 v[124:125], v[144:145], v[152:153] op_sel_hi:[1,0]
	v_pk_mul_f32 v[126:127], v[146:147], v[152:153] op_sel_hi:[1,0]
	s_waitcnt vmcnt(7)
	v_pk_mul_f32 v[122:123], v[124:125], v[238:239]
	v_pk_mul_f32 v[120:121], v[126:127], v[236:237]
	v_lshlrev_b32_e32 v124, 4, v48
	global_store_dwordx4 v124, v[120:123], s[12:13]
	s_nop 0
	v_pk_mul_f32 v[124:125], v[148:149], v[152:153] op_sel_hi:[1,0]
	v_pk_mul_f32 v[126:127], v[150:151], v[152:153] op_sel_hi:[1,0]
	s_waitcnt vmcnt(7)
	v_pk_mul_f32 v[122:123], v[124:125], v[242:243]
	v_pk_mul_f32 v[120:121], v[126:127], v[240:241]
	v_lshlrev_b32_e32 v124, 4, v52
	global_store_dwordx4 v124, v[120:123], s[12:13]
